# P4 split: even workgroups attention then conversion, odd workgroups conversion then attention (two tiles in flight per wave in every conversion); P6-idle CUs host items [24576,39168); nt loads
# baseline (speedup 1.0000x reference)
; __global__ void __launch_bounds__(NWAVES * 64, 2) mk_fwd(Args args) {
;     ...
;         const int NCONV = (CONV_OVERLAP && G >= 128) ? 51 : 0;
;         if (bx < NCONV) convert_weights<false, true>(P, lds, bx * NWAVES + wave, NCONV * NWAVES, wave, lane, 0, (CONV_OVERLAP && G >= 192) ? LATE_SPLIT : 0x7fffffff);
;         else {
;             sb_phase(lds, PROJ, (bf16*)(ws + WS_MIX), (const float*)(ws + WS_RSB), P.sbo_norm, bx - NCONV, G - NCONV, tid);
;             ret_out_phase(lds, PROJ, (bf16*)(ws + WS_MIX), (const bf16*)(ws + WS_ST), P.ret_norm, bx - NCONV, G - NCONV, tid);
;         }
;         if (NCONV == 0) convert_weights<false>(P, lds, gw, NGW, wave, lane);
.LBB0_519:
	s_mov_b32 s98, 0
	s_and_b32 s99, s2, 1
	s_mov_b32 s100, s80
	s_mov_b32 s101, s56
	v_writelane_b32 v255, s70, 4
	v_writelane_b32 v255, s71, 5
	s_mov_b32 s0, 0x9900
	s_cmp_eq_u32 s80, 0x100
	s_cselect_b32 s1, 1, 0
	s_cmp_gt_i32 s75, 6
	s_cselect_b32 s1, s1, 0
	s_cmp_lg_u32 s1, 0
	s_cselect_b32 s0, 0x6000, s0
	v_writelane_b32 v255, s0, 2
	s_mov_b32 s0, 0
	v_writelane_b32 v255, s0, 3

; #define GAS __attribute__((address_space(1)))
; template <bool UNCOND> DI void witem_load(const WItem& d, WRegs& R, int lane) {
;     const int n4 = lane & 31, kh = lane >> 5;
;     const float* src = d.W + (size_t)(d.k0 + 2 * kh) * d.N + d.src_col0 + 4 * n4;
; #pragma unroll
;     for (int i = 0; i < 8; ++i) { R.a[i] = *(const GAS f32x4*)(src + (size_t)(4 * i) * d.N); R.b[i] = *(const GAS f32x4*)(src + (size_t)(4 * i + 1) * d.N); }
;     if (UNCOND) {
;         const float* gp = d.gain ? d.gain + d.k0 + 2 * kh : src;
; #pragma unroll
;         for (int i = 0; i < 8; ++i) R.gg[i] = *(const GAS f32x2g*)(gp + 4 * i);
;         if (!d.gain) {
; #pragma unroll
;             for (int i = 0; i < 8; ++i) R.gg[i] = (f32x2g){1.f, 1.f}; }
;     } else if (d.gain) {
; #pragma unroll
;         for (int i = 0; i < 8; ++i) R.gg[i] = *(const GAS f32x2g*)(d.gain + d.k0 + 4 * i + 2 * kh); }
;     else {
; #pragma unroll
;         for (int i = 0; i < 8; ++i) R.gg[i] = (f32x2g){1.f, 1.f}; }
.LBB0_611:
	v_cndmask_b32_e64 v150, 0, 1, s[4:5]
	v_cmp_ne_u32_e64 s[0:1], 1, v150
	s_andn2_b64 vcc, exec, s[4:5]
	s_mov_b32 s100, 0
	s_cbranch_vccnz .LBB0_615
	v_add_u32_e32 v66, s36, v146
	v_mad_i64_i32 v[66:67], s[4:5], s38, v66, 0
	v_lshl_add_u64 v[66:67], v[66:67], 2, s[30:31]
	s_ashr_i32 s43, s42, 31
	s_ashr_i32 s39, s38, 31
	v_lshl_add_u64 v[66:67], s[42:43], 2, v[66:67]
	v_lshlrev_b32_e32 v150, 2, v148
	v_lshl_add_u64 v[66:67], v[66:67], 0, v[150:151]
	s_lshl_b64 s[4:5], s[38:39], 2
	v_lshl_add_u64 v[70:71], v[66:67], 0, s[4:5]
	global_load_dwordx4 v[66:69], v[66:67], off nt
	s_nop 0
	global_load_dwordx4 v[74:77], v[70:71], off nt
	v_mad_i64_i32 v[70:71], s[6:7], s38, 12, v[70:71]
	v_lshl_add_u64 v[78:79], v[70:71], 0, s[4:5]
	global_load_dwordx4 v[70:73], v[70:71], off nt
	s_nop 0
	global_load_dwordx4 v[82:85], v[78:79], off nt
	v_mad_i64_i32 v[78:79], s[6:7], s38, 12, v[78:79]
	v_lshl_add_u64 v[86:87], v[78:79], 0, s[4:5]
	global_load_dwordx4 v[78:81], v[78:79], off nt
	s_nop 0
	global_load_dwordx4 v[90:93], v[86:87], off nt
	v_mad_i64_i32 v[86:87], s[6:7], s38, 12, v[86:87]
	v_lshl_add_u64 v[94:95], v[86:87], 0, s[4:5]
	v_mad_i64_i32 v[102:103], s[6:7], s38, 12, v[94:95]
	global_load_dwordx4 v[86:89], v[86:87], off nt
	s_nop 0
	global_load_dwordx4 v[98:101], v[94:95], off nt
	s_cmp_eq_u64 s[34:35], 0
	global_load_dwordx4 v[94:97], v[102:103], off nt
	v_lshl_add_u64 v[102:103], v[102:103], 0, s[4:5]
	v_mad_i64_i32 v[110:111], s[6:7], s38, 12, v[102:103]
	global_load_dwordx4 v[106:109], v[102:103], off nt
	s_nop 0
	global_load_dwordx4 v[102:105], v[110:111], off nt
	v_lshl_add_u64 v[110:111], v[110:111], 0, s[4:5]
	v_mad_i64_i32 v[118:119], s[6:7], s38, 12, v[110:111]
	global_load_dwordx4 v[114:117], v[110:111], off nt
	s_nop 0
	global_load_dwordx4 v[110:113], v[118:119], off nt
	v_lshl_add_u64 v[118:119], v[118:119], 0, s[4:5]
	v_mad_i64_i32 v[126:127], s[6:7], s38, 12, v[118:119]
	global_load_dwordx4 v[122:125], v[118:119], off nt
	s_nop 0
	global_load_dwordx4 v[118:121], v[126:127], off nt
	v_lshl_add_u64 v[126:127], v[126:127], 0, s[4:5]
	global_load_dwordx4 v[126:129], v[126:127], off nt
	s_cbranch_scc1 .LBB0_614
	s_ashr_i32 s37, s36, 31
	s_lshl_b64 s[4:5], s[36:37], 2
	s_add_u32 s4, s34, s4
	s_addc_u32 s5, s35, s5
	v_lshlrev_b32_e32 v150, 2, v146
	s_mul_i32 s100, s99, 24
	global_load_dwordx2 v[152:153], v150, s[4:5]
	global_load_dwordx2 v[154:155], v150, s[4:5] offset:16
	global_load_dwordx2 v[156:157], v150, s[4:5] offset:32
	global_load_dwordx2 v[158:159], v150, s[4:5] offset:48
	global_load_dwordx2 v[160:161], v150, s[4:5] offset:64
	global_load_dwordx2 v[162:163], v150, s[4:5] offset:80
	global_load_dwordx2 v[164:165], v150, s[4:5] offset:96
	global_load_dwordx2 v[166:167], v150, s[4:5] offset:112
	s_branch .LBB0_615
.LBB0_614:
	s_mul_i32 s100, s99, 16
	v_mov_b32_e32 v153, 1.0
	v_mov_b32_e32 v152, v153
	v_mov_b32_e32 v155, v153
	v_mov_b32_e32 v154, v153
	v_mov_b32_e32 v157, v153
	v_mov_b32_e32 v156, v153
	v_mov_b32_e32 v159, v153
	v_mov_b32_e32 v158, v153
	v_mov_b32_e32 v161, v153
	v_mov_b32_e32 v160, v153
	v_mov_b32_e32 v163, v153
	v_mov_b32_e32 v162, v153
	v_mov_b32_e32 v165, v153
	v_mov_b32_e32 v164, v153
	v_mov_b32_e32 v167, v153
	v_mov_b32_e32 v166, v153

; #define GAS __attribute__((address_space(1)))
; template <bool UNCOND> DI void witem_load(const WItem& d, WRegs& R, int lane) {
;     const int n4 = lane & 31, kh = lane >> 5;
;     const float* src = d.W + (size_t)(d.k0 + 2 * kh) * d.N + d.src_col0 + 4 * n4;
; #pragma unroll
;     for (int i = 0; i < 8; ++i) { R.a[i] = *(const GAS f32x4*)(src + (size_t)(4 * i) * d.N); R.b[i] = *(const GAS f32x4*)(src + (size_t)(4 * i + 1) * d.N); }
;     if (UNCOND) {
;         const float* gp = d.gain ? d.gain + d.k0 + 2 * kh : src;
; #pragma unroll
;         for (int i = 0; i < 8; ++i) R.gg[i] = *(const GAS f32x2g*)(gp + 4 * i);
;         if (!d.gain) {
; #pragma unroll
;             for (int i = 0; i < 8; ++i) R.gg[i] = (f32x2g){1.f, 1.f}; }
;     } else if (d.gain) {
; #pragma unroll
;         for (int i = 0; i < 8; ++i) R.gg[i] = *(const GAS f32x2g*)(d.gain + d.k0 + 4 * i + 2 * kh); }
;     else {
; #pragma unroll
;         for (int i = 0; i < 8; ++i) R.gg[i] = (f32x2g){1.f, 1.f}; }
.LBB0_679:
	s_andn2_b64 vcc, exec, s[0:1]
	s_mov_b32 s100, 0
	s_cbranch_vccnz .LBB0_683
	v_add_u32_e32 v2, s14, v146
	v_mad_i64_i32 v[2:3], s[0:1], s16, v2, 0
	v_lshl_add_u64 v[2:3], v[2:3], 2, s[8:9]
	s_ashr_i32 s19, s18, 31
	s_ashr_i32 s17, s16, 31
	v_lshl_add_u64 v[2:3], s[18:19], 2, v[2:3]
	v_lshlrev_b32_e32 v150, 2, v148
	v_lshl_add_u64 v[2:3], v[2:3], 0, v[150:151]
	s_lshl_b64 s[0:1], s[16:17], 2
	v_lshl_add_u64 v[10:11], v[2:3], 0, s[0:1]
	global_load_dwordx4 v[6:9], v[2:3], off nt
	s_nop 0
	global_load_dwordx4 v[2:5], v[10:11], off nt
	v_mad_i64_i32 v[10:11], s[4:5], s16, 12, v[10:11]
	v_lshl_add_u64 v[18:19], v[10:11], 0, s[0:1]
	global_load_dwordx4 v[14:17], v[10:11], off nt
	s_nop 0
	global_load_dwordx4 v[10:13], v[18:19], off nt
	v_mad_i64_i32 v[18:19], s[4:5], s16, 12, v[18:19]
	v_lshl_add_u64 v[26:27], v[18:19], 0, s[0:1]
	global_load_dwordx4 v[22:25], v[18:19], off nt
	s_nop 0
	global_load_dwordx4 v[18:21], v[26:27], off nt
	v_mad_i64_i32 v[26:27], s[4:5], s16, 12, v[26:27]
	v_lshl_add_u64 v[34:35], v[26:27], 0, s[0:1]
	global_load_dwordx4 v[30:33], v[26:27], off nt
	s_nop 0
	global_load_dwordx4 v[26:29], v[34:35], off nt
	v_mad_i64_i32 v[34:35], s[4:5], s16, 12, v[34:35]
	v_lshl_add_u64 v[42:43], v[34:35], 0, s[0:1]
	global_load_dwordx4 v[38:41], v[34:35], off nt
	s_cmp_eq_u64 s[10:11], 0
	global_load_dwordx4 v[34:37], v[42:43], off nt
	v_mad_i64_i32 v[42:43], s[4:5], s16, 12, v[42:43]
	v_lshl_add_u64 v[50:51], v[42:43], 0, s[0:1]
	global_load_dwordx4 v[46:49], v[42:43], off nt
	s_nop 0
	global_load_dwordx4 v[42:45], v[50:51], off nt
	v_mad_i64_i32 v[50:51], s[4:5], s16, 12, v[50:51]
	v_lshl_add_u64 v[58:59], v[50:51], 0, s[0:1]
	global_load_dwordx4 v[54:57], v[50:51], off nt
	s_nop 0
	global_load_dwordx4 v[50:53], v[58:59], off nt
	v_mad_i64_i32 v[58:59], s[4:5], s16, 12, v[58:59]
	global_load_dwordx4 v[62:65], v[58:59], off nt
	v_lshl_add_u64 v[58:59], v[58:59], 0, s[0:1]
	global_load_dwordx4 v[58:61], v[58:59], off nt
	s_cbranch_scc1 .LBB0_682
	s_ashr_i32 s15, s14, 31
	s_lshl_b64 s[0:1], s[14:15], 2
	s_add_u32 s0, s10, s0
	s_addc_u32 s1, s11, s1
	v_lshlrev_b32_e32 v144, 2, v146
	s_mul_i32 s100, s99, 24
	global_load_dwordx2 v[130:131], v144, s[0:1]
	global_load_dwordx2 v[132:133], v144, s[0:1] offset:16
	global_load_dwordx2 v[134:135], v144, s[0:1] offset:32
	global_load_dwordx2 v[136:137], v144, s[0:1] offset:48
	global_load_dwordx2 v[138:139], v144, s[0:1] offset:64
	global_load_dwordx2 v[140:141], v144, s[0:1] offset:80
	global_load_dwordx2 v[142:143], v144, s[0:1] offset:96
	s_nop 0
	global_load_dwordx2 v[144:145], v144, s[0:1] offset:112
	s_branch .LBB0_683
.LBB0_682:
	s_mul_i32 s100, s99, 16
	v_mov_b32_e32 v131, 1.0
	v_mov_b32_e32 v130, v131
	v_mov_b32_e32 v133, v131
	v_mov_b32_e32 v132, v131
	v_mov_b32_e32 v135, v131
	v_mov_b32_e32 v134, v131
	v_mov_b32_e32 v137, v131
	v_mov_b32_e32 v136, v131
	v_mov_b32_e32 v139, v131
	v_mov_b32_e32 v138, v131
	v_mov_b32_e32 v141, v131
	v_mov_b32_e32 v140, v131
	v_mov_b32_e32 v143, v131
	v_mov_b32_e32 v142, v131
	v_mov_b32_e32 v145, v131
	v_mov_b32_e32 v144, v131

; __global__ void __launch_bounds__(NWAVES * 64, 2) mk_fwd(Args args) {
;     ...
;         if (bx < NCONV) convert_weights<false, true>(P, lds, bx * NWAVES + wave, NCONV * NWAVES, wave, lane, 0, (CONV_OVERLAP && G >= 192) ? LATE_SPLIT : 0x7fffffff);
;         else {
;             sb_phase(lds, PROJ, (bf16*)(ws + WS_MIX), (const float*)(ws + WS_RSB), P.sbo_norm, bx - NCONV, G - NCONV, tid);
;             ret_out_phase(lds, PROJ, (bf16*)(ws + WS_MIX), (const bf16*)(ws + WS_ST), P.ret_norm, bx - NCONV, G - NCONV, tid);
;         }
;         if (NCONV == 0) convert_weights<false>(P, lds, gw, NGW, wave, lane);
;         __syncthreads();
.LBB0_727:
	s_waitcnt vmcnt(0) lgkmcnt(0)
	s_barrier
	s_cmp_eq_u32 s98, 2
	s_cbranch_scc1 .Lp6_conv_ret
	s_cmp_eq_u32 s98, 1
	s_cbranch_scc1 .Lp4_done
	s_mov_b32 s98, 1
	s_xor_b32 s99, s99, 1
	s_mov_b32 s100, s80
	v_readlane_b32 s70, v255, 4
	v_readlane_b32 s71, v255, 5
	s_mov_b64 s[4:5], -1
	s_add_u32 s42, s84, 0x26e00000
	s_addc_u32 s43, s85, 0
	s_nop 1
	s_load_dwordx2 s[44:45], s[70:71], 0x20
	s_load_dwordx2 s[50:51], s[70:71], 0x38
	s_waitcnt lgkmcnt(0)
	s_branch .Lp4_conv_entry

; __global__ void __launch_bounds__(NWAVES * 64, 2) mk_fwd(Args args) {
;     ...
;         if (CONV_OVERLAP && G >= 192 && bx >= G / 2 + 8) { __syncthreads(); convert_weights<false, true>(P, lds, (bx - (G / 2 + 8)) * NWAVES + wave, (G - (G / 2 + 8)) * NWAVES, wave, lane, LATE_SPLIT, 0x7fffffff); }
.LBB0_925:
	s_cmpk_lt_i32 s2, 0x88
	s_cbranch_scc1 .Lp6_hook_done
	s_cmp_lg_u32 s80, 0x100
	s_cbranch_scc1 .Lp6_hook_done
	s_cmp_gt_i32 s74, 4
	s_cbranch_scc1 .Lp6_hook_done
	s_cmp_lt_i32 s75, 7
	s_cbranch_scc1 .Lp6_hook_done
	v_writelane_b32 v255, s8, 8
	v_writelane_b32 v255, s9, 9
	v_writelane_b32 v255, s12, 10
	v_writelane_b32 v255, s16, 11
	v_writelane_b32 v255, s18, 12
	v_writelane_b32 v255, s19, 13
	v_writelane_b32 v255, s20, 14
	v_writelane_b32 v255, s21, 15
	v_writelane_b32 v255, s23, 16
	v_writelane_b32 v255, s24, 17
	v_writelane_b32 v255, s26, 18
	v_writelane_b32 v255, s34, 19
	v_readlane_b32 s70, v254, 0
	v_readlane_b32 s71, v254, 1
	v_and_b32_e32 v1, 63, v0
	v_readfirstlane_b32 s101, v0
	s_sub_u32 s100, s2, 0x88
	s_lshl_b32 s100, s100, 3
	s_sub_u32 s70, s70, 0xc0
	s_subb_u32 s71, s71, 0
	s_lshr_b32 s101, s101, 6
	s_add_u32 s101, s101, s100
	s_mov_b32 s100, 120
	s_mov_b32 s0, 0x3900
	v_writelane_b32 v255, s0, 2
	s_mov_b32 s0, 0x6000
	v_writelane_b32 v255, s0, 3
	s_mov_b32 s98, 2
	s_mov_b32 s99, 1
	s_mov_b64 s[4:5], -1
	s_branch .Lp4_conv_entry
